# v27 with the cross-half row-max copy issued ahead of the last P.V MFMA (MFMA as the permlane wait state)
# baseline (speedup 1.0000x reference)
.LBB0_1235:
	s_add_i32 s15, s14, 1
	s_cmp_lg_u32 s14, 2
	s_cselect_b32 s14, s15, 0
	s_mul_i32 s15, s14, 0x6400
	v_add_u32_e32 v70, s15, v185
	ds_read_b128 v[66:69], v70
	ds_read_b128 v[166:169], v70 offset:32
	ds_read_b128 v[170:173], v70 offset:64
	ds_read_b128 v[188:191], v70 offset:96
	ds_read_b128 v[192:195], v70 offset:128
	ds_read_b128 v[196:199], v70 offset:160
	ds_read_b128 v[200:203], v70 offset:192
	ds_read_b128 v[216:219], v70 offset:224
	ds_read_b128 v[220:223], v70 offset:256
	ds_read_b128 v[224:227], v70 offset:288
	ds_read_b128 v[228:231], v70 offset:320
	ds_read_b128 v[146:149], v70 offset:352
	s_waitcnt lgkmcnt(11)
	v_mfma_f32_32x32x16_bf16 v[66:81], v[66:69], v[142:145], 0
	v_sub_f32_e32 v82, v82, v183
	v_exp_f32_e32 v82, v82
	v_sub_f32_e32 v94, v94, v183
	v_exp_f32_e32 v94, v94
	v_add_f32_e32 v165, 0, v82
	v_add_f32_e32 v165, v94, v165
	s_waitcnt lgkmcnt(10)
	v_mfma_f32_32x32x16_bf16 v[66:81], v[166:169], v[138:141], v[66:81]
	v_sub_f32_e32 v83, v83, v183
	v_exp_f32_e32 v83, v83
	v_sub_f32_e32 v95, v95, v183
	v_exp_f32_e32 v95, v95
	v_add_f32_e32 v165, v83, v165
	v_cvt_pk_bf16_f32 v82, v82, v83
	v_add_f32_e32 v165, v95, v165
	v_sub_f32_e32 v83, v84, v183
	s_waitcnt lgkmcnt(9)
	v_mfma_f32_32x32x16_bf16 v[66:81], v[170:173], v[134:137], v[66:81]
	v_exp_f32_e32 v83, v83
	v_sub_f32_e32 v96, v96, v183
	v_add_f32_e32 v84, v83, v165
	v_exp_f32_e32 v165, v96
	s_nop 0
	v_add_f32_e32 v84, v165, v84
	s_waitcnt lgkmcnt(8)
	v_mfma_f32_32x32x16_bf16 v[66:81], v[188:191], v[130:133], v[66:81]
	v_sub_f32_e32 v85, v85, v183
	v_exp_f32_e32 v85, v85
	v_sub_f32_e32 v96, v97, v183
	v_exp_f32_e32 v97, v96
	v_cvt_pk_bf16_f32 v96, v94, v95
	v_add_f32_e32 v84, v85, v84
	v_cvt_pk_bf16_f32 v83, v83, v85
	v_add_f32_e32 v84, v97, v84
	v_cvt_pk_bf16_f32 v97, v165, v97
	s_waitcnt lgkmcnt(7)
	v_mfma_f32_32x32x16_bf16 v[66:81], v[192:195], v[126:129], v[66:81]
	v_sub_f32_e32 v85, v86, v183
	v_exp_f32_e32 v85, v85
	s_nop 0
	v_add_f32_e32 v84, v85, v84
	s_waitcnt lgkmcnt(6)
	v_mfma_f32_32x32x16_bf16 v[66:81], v[196:199], v[122:125], v[66:81]
	v_sub_f32_e32 v86, v87, v183
	v_exp_f32_e32 v86, v86
	s_nop 0
	v_add_f32_e32 v87, v86, v84
	v_cvt_pk_bf16_f32 v84, v85, v86
	s_waitcnt lgkmcnt(5)
	v_mfma_f32_32x32x16_bf16 v[66:81], v[200:203], v[118:121], v[66:81]
	v_sub_f32_e32 v85, v88, v183
	v_exp_f32_e32 v85, v85
	s_nop 0
	v_add_f32_e32 v86, v85, v87
	s_waitcnt lgkmcnt(4)
	v_mfma_f32_32x32x16_bf16 v[66:81], v[216:219], v[114:117], v[66:81]
	v_sub_f32_e32 v87, v89, v183
	v_exp_f32_e32 v87, v87
	s_nop 0
	v_add_f32_e32 v86, v87, v86
	v_cvt_pk_bf16_f32 v85, v85, v87
	v_sub_f32_e32 v87, v90, v183
	v_exp_f32_e32 v90, v87
	s_waitcnt lgkmcnt(3)
	v_mfma_f32_32x32x16_bf16 v[66:81], v[220:223], v[110:113], v[66:81]
	v_add_u32_e32 v165, s13, v187
	v_add_f32_e32 v94, v90, v86
	ds_read_b128 v[86:89], v165
	ds_read_b128 v[166:169], v165 offset:32
	s_waitcnt lgkmcnt(4)
	v_mfma_f32_32x32x16_bf16 v[66:81], v[224:227], v[106:109], v[66:81]
	v_sub_f32_e32 v91, v91, v183
	ds_read_b128 v[170:173], v165 offset:4608
	ds_read_b128 v[188:191], v165 offset:4640
	v_exp_f32_e32 v91, v91
	s_nop 0
	v_add_f32_e32 v95, v91, v94
	v_cvt_pk_bf16_f32 v94, v90, v91
	s_waitcnt lgkmcnt(5)
	v_mfma_f32_32x32x16_bf16 v[66:81], v[228:231], v[102:105], v[66:81]
	v_sub_f32_e32 v90, v92, v183
	ds_read_b128 v[192:195], v165 offset:9216
	ds_read_b128 v[196:199], v165 offset:9248
	v_exp_f32_e32 v90, v90
	s_nop 0
	v_add_f32_e32 v91, v90, v95
	v_sub_f32_e32 v92, v93, v183
	v_exp_f32_e32 v92, v92
	s_waitcnt lgkmcnt(6)
	v_mfma_f32_32x32x16_bf16 v[66:81], v[146:149], v[98:101], v[66:81]
	v_add_f32_e32 v186, v92, v91
	v_cvt_pk_bf16_f32 v95, v90, v92
	ds_read_b128 v[90:93], v165 offset:13824
	ds_read_b128 v[146:149], v165 offset:13856
	s_orn2_b64 vcc, s[0:1], s[24:25]
	s_and_b64 vcc, vcc, exec
	s_cbranch_vccnz .LattB_slow
	s_mul_i32 s13, s12, 0x6400
	s_add_u32 s16, s80, s2
	s_addc_u32 s17, s81, s3
	s_add_u32 s16, s16, 0x30e90000
	s_addc_u32 s17, s17, 0
	s_waitcnt lgkmcnt(0)
	v_mfma_f32_32x32x16_bf16 v[50:65], v[86:89], v[82:85], v[50:65]
	v_add_f32_e32 v186, v164, v186
	s_add_i32 m0, s13, s65
	s_nop 0
	global_load_lds_dwordx4 v208, s[16:17]
	v_mfma_f32_32x32x16_bf16 v[34:49], v[170:173], v[82:85], v[34:49]
	s_add_i32 m0, s13, s66
	s_nop 0
	global_load_lds_dwordx4 v209, s[16:17]
	v_mfma_f32_32x32x16_bf16 v[18:33], v[192:195], v[82:85], v[18:33]
	v_max_f32_e32 v150, v66, v67
	v_max3_f32 v150, v150, v68, v69
	s_add_i32 m0, s13, s67
	s_add_i32 s13, s13, s68
	global_load_lds_dwordx4 v210, s[16:17]
	v_mfma_f32_32x32x16_bf16 v[2:17], v[90:93], v[82:85], v[2:17]
	v_max3_f32 v150, v150, v70, v71
	v_max3_f32 v150, v150, v72, v73
	s_add_i32 m0, s13, 0x6000
	s_nop 0
	global_load_lds_dwordx4 v211, s[16:17]
	v_mfma_f32_32x32x16_bf16 v[50:65], v[166:169], v[94:97], v[50:65]
	v_max3_f32 v150, v150, v74, v75
	v_max3_f32 v150, v150, v76, v77
	s_mul_i32 s13, s12, 0x4800
	s_add_i32 s15, s13, 0xffffb800
	s_cmp_lg_u32 s12, 0
	s_cselect_b32 s15, s15, 0x9000
	s_add_i32 s15, s15, 0x12c00
	s_add_u32 s16, s82, s2
	s_addc_u32 s17, s83, s3
	s_add_u32 s16, s16, 0x31bf8180
	s_addc_u32 s17, s17, 0
	s_add_i32 m0, s15, s69
	s_nop 0
	global_load_lds_dwordx4 v212, s[16:17]
	v_mfma_f32_32x32x16_bf16 v[34:49], v[188:191], v[94:97], v[34:49]
	v_max3_f32 v150, v150, v78, v79
	v_max3_f32 v150, v150, v80, v81
	s_add_i32 m0, s15, s70
	s_nop 0
	global_load_lds_dwordx4 v213, s[16:17]
	v_mfma_f32_32x32x16_bf16 v[18:33], v[196:199], v[94:97], v[18:33]
	s_add_i32 m0, s15, s71
	s_nop 0
	global_load_lds_dwordx4 v214, s[16:17]
	v_mov_b32_e32 v151, v150
	v_mfma_f32_32x32x16_bf16 v[2:17], v[146:149], v[94:97], v[2:17]
	s_nop 0
	v_permlane32_swap_b32_e32 v151, v150
	v_max_f32_e32 v150, v150, v151
	s_branch .LattB_join

.LBB0_1240:
	s_mul_i32 s13, s14, 0x6400
	v_add_u32_e32 v86, s13, v185
	ds_read_b128 v[82:85], v86
	ds_read_b128 v[188:191], v86 offset:32
	ds_read_b128 v[192:195], v86 offset:64
	ds_read_b128 v[196:199], v86 offset:96
	ds_read_b128 v[200:203], v86 offset:128
	ds_read_b128 v[216:219], v86 offset:160
	ds_read_b128 v[220:223], v86 offset:192
	ds_read_b128 v[224:227], v86 offset:224
	ds_read_b128 v[228:231], v86 offset:256
	ds_read_b128 v[232:235], v86 offset:288
	ds_read_b128 v[236:239], v86 offset:320
	ds_read_b128 v[240:243], v86 offset:352
	s_waitcnt lgkmcnt(11)
	v_mfma_f32_32x32x16_bf16 v[82:97], v[82:85], v[142:145], 0
	v_sub_f32_e32 v66, v66, v183
	v_sub_f32_e32 v78, v78, v183
	v_exp_f32_e32 v66, v66
	v_exp_f32_e32 v78, v78
	s_waitcnt lgkmcnt(10)
	v_mfma_f32_32x32x16_bf16 v[82:97], v[188:191], v[138:141], v[82:97]
	v_sub_f32_e32 v67, v67, v183
	v_sub_f32_e32 v79, v79, v183
	v_exp_f32_e32 v67, v67
	v_exp_f32_e32 v79, v79
	v_cvt_pk_bf16_f32 v188, v66, v67
	s_waitcnt lgkmcnt(9)
	v_mfma_f32_32x32x16_bf16 v[82:97], v[192:195], v[134:137], v[82:97]
	v_sub_f32_e32 v68, v68, v183
	v_sub_f32_e32 v80, v80, v183
	v_exp_f32_e32 v68, v68
	v_exp_f32_e32 v80, v80
	s_waitcnt lgkmcnt(8)
	v_mfma_f32_32x32x16_bf16 v[82:97], v[196:199], v[130:133], v[82:97]
	v_sub_f32_e32 v69, v69, v183
	v_sub_f32_e32 v81, v81, v183
	v_exp_f32_e32 v69, v69
	v_exp_f32_e32 v81, v81
	v_cvt_pk_bf16_f32 v194, v78, v79
	v_cvt_pk_bf16_f32 v189, v68, v69
	v_cvt_pk_bf16_f32 v195, v80, v81
	s_waitcnt lgkmcnt(7)
	v_mfma_f32_32x32x16_bf16 v[82:97], v[200:203], v[126:129], v[82:97]
	v_sub_f32_e32 v70, v70, v183
	v_exp_f32_e32 v70, v70
	s_waitcnt lgkmcnt(6)
	v_mfma_f32_32x32x16_bf16 v[82:97], v[216:219], v[122:125], v[82:97]
	v_sub_f32_e32 v71, v71, v183
	v_exp_f32_e32 v71, v71
	s_nop 0
	v_cvt_pk_bf16_f32 v190, v70, v71
	s_waitcnt lgkmcnt(5)
	v_mfma_f32_32x32x16_bf16 v[82:97], v[220:223], v[118:121], v[82:97]
	v_sub_f32_e32 v72, v72, v183
	v_exp_f32_e32 v72, v72
	s_waitcnt lgkmcnt(4)
	v_mfma_f32_32x32x16_bf16 v[82:97], v[224:227], v[114:117], v[82:97]
	v_sub_f32_e32 v73, v73, v183
	v_exp_f32_e32 v73, v73
	s_nop 0
	v_cvt_pk_bf16_f32 v191, v72, v73
	s_waitcnt lgkmcnt(3)
	v_mfma_f32_32x32x16_bf16 v[82:97], v[228:231], v[110:113], v[82:97]
	v_add_u32_e32 v204, s12, v187
	v_sub_f32_e32 v74, v74, v183
	ds_read_b128 v[196:199], v204
	ds_read_b128 v[200:203], v204 offset:32
	v_exp_f32_e32 v74, v74
	s_waitcnt lgkmcnt(4)
	v_mfma_f32_32x32x16_bf16 v[82:97], v[232:235], v[106:109], v[82:97]
	v_sub_f32_e32 v75, v75, v183
	ds_read_b128 v[216:219], v204 offset:4608
	ds_read_b128 v[220:223], v204 offset:4640
	v_exp_f32_e32 v75, v75
	s_nop 0
	v_cvt_pk_bf16_f32 v192, v74, v75
	s_waitcnt lgkmcnt(5)
	v_mfma_f32_32x32x16_bf16 v[82:97], v[236:239], v[102:105], v[82:97]
	v_sub_f32_e32 v76, v76, v183
	ds_read_b128 v[224:227], v204 offset:9216
	ds_read_b128 v[228:231], v204 offset:9248
	v_exp_f32_e32 v76, v76
	s_waitcnt lgkmcnt(6)
	v_mfma_f32_32x32x16_bf16 v[82:97], v[240:243], v[98:101], v[82:97]
	v_sub_f32_e32 v77, v77, v183
	ds_read_b128 v[232:235], v204 offset:13824
	ds_read_b128 v[236:239], v204 offset:13856
	v_exp_f32_e32 v77, v77
	s_nop 0
	v_cvt_pk_bf16_f32 v193, v76, v77
	s_and_b64 vcc, exec, s[0:1]
	s_cbranch_vccnz .LattA_slow
	s_mul_i32 s12, s36, 0x6400
	s_add_u32 s16, s80, s2
	s_addc_u32 s17, s81, s3
	s_add_u32 s16, s16, 0x30e8a000
	s_addc_u32 s17, s17, 0
	s_waitcnt lgkmcnt(0)
	v_mfma_f32_32x32x16_bf16 v[50:65], v[196:199], v[188:191], v[50:65]
	s_add_i32 m0, s12, s65
	s_nop 0
	global_load_lds_dwordx4 v208, s[16:17]
	v_mfma_f32_32x32x16_bf16 v[34:49], v[216:219], v[188:191], v[34:49]
	s_add_i32 m0, s12, s66
	s_nop 0
	global_load_lds_dwordx4 v209, s[16:17]
	v_mfma_f32_32x32x16_bf16 v[18:33], v[224:227], v[188:191], v[18:33]
	v_max_f32_e32 v152, v82, v83
	v_max3_f32 v152, v152, v84, v85
	s_add_i32 m0, s12, s67
	s_add_i32 s12, s12, s68
	global_load_lds_dwordx4 v210, s[16:17]
	v_mfma_f32_32x32x16_bf16 v[2:17], v[232:235], v[188:191], v[2:17]
	v_max3_f32 v152, v152, v86, v87
	v_max3_f32 v152, v152, v88, v89
	s_add_i32 m0, s12, 0x6000
	s_nop 0
	global_load_lds_dwordx4 v211, s[16:17]
	v_mfma_f32_32x32x16_bf16 v[50:65], v[200:203], v[192:195], v[50:65]
	v_max3_f32 v152, v152, v90, v91
	v_max3_f32 v152, v152, v92, v93
	s_mul_i32 s12, s36, 0x4800
	s_add_i32 s13, s12, 0xffffb800
	s_cmp_lg_u32 s36, 0
	s_cselect_b32 s13, s13, 0x9000
	s_add_i32 s13, s13, 0x12c00
	s_add_u32 s16, s82, s2
	s_addc_u32 s17, s83, s3
	s_add_u32 s16, s16, s28
	s_addc_u32 s17, s17, s29
	s_add_i32 m0, s13, s69
	s_nop 0
	global_load_lds_dwordx4 v212, s[16:17]
	v_mfma_f32_32x32x16_bf16 v[34:49], v[220:223], v[192:195], v[34:49]
	v_max3_f32 v152, v152, v94, v95
	v_max3_f32 v152, v152, v96, v97
	s_add_i32 m0, s13, s70
	s_nop 0
	global_load_lds_dwordx4 v213, s[16:17]
	v_mfma_f32_32x32x16_bf16 v[18:33], v[228:231], v[192:195], v[18:33]
	s_add_i32 m0, s13, s71
	s_nop 0
	global_load_lds_dwordx4 v214, s[16:17]
	v_mov_b32_e32 v153, v152
	v_mfma_f32_32x32x16_bf16 v[2:17], v[236:239], v[192:195], v[2:17]
	s_nop 0
	v_permlane32_swap_b32_e32 v153, v152
	v_max_f32_e32 v152, v152, v153
	s_branch .LattA_join
